# v58 plus AT_ISSUE list reads batched into one lane-parallel LDS read (E4)
# baseline (speedup 1.0000x reference)
; #define LAS __attribute__((address_space(3)))
;     ...
;             const unsigned kthr = (unsigned)(c.tid >> 3) * (unsigned)kstride + (unsigned)(c.tid & 7) * 8u, vthr = (unsigned)(c.tid >> 3) * (unsigned)vstride + (unsigned)(c.tid & 7) * 8u;
;             int st_k, st_va;
;             { const int row = c.tid >> 3, cj = c.tid & 7, ga = 2 * cj;
;               st_k = row * 128 + (((cj ^ row) & 7) << 4);
;               st_va = row * 128 + (((((ga >> 3) * 4 + (ga & 3)) ^ row) & 7) << 4) + ((ga >> 2) & 1) * 8; }
;             u32x4 kreg[TS], vreg[TS]; int p0n[TS];
;             const int nrounds = (ntiles + TS - 1) / TS;
;             if (nrounds > 0) AT_ISSUE(0);
;             if (pass == 0) {
;                 for (int e = c.tid; e < 4 * NT; e += 512) { const int r = e / NT, dist = DOFF - (e - r * NT); const bool vis = dist >= 0 && (MODE != 0 || dist < 128) && (MODE != 1 || dist < 512);
;                     biasd[e] = vis ? reltab[t5_bucket(dist > 1023 ? 1023 : dist) * 16 + (MODE == 0 ? 8 : 0) + g * 4 + r] : -1e30f; } }
;             for (int rd = 0; rd < nrounds; ++rd) {
;                 int p0s[TS];
; #pragma unroll
;                 for (int i = 0; i < TS; ++i) p0s[i] = p0n[i];
;                 __syncthreads();
; #pragma unroll
;                 for (int i = 0; i < TS; ++i) {
;                     *(LAS u32x4*)(L + AT_K + i * AT_TS + st_k) = kreg[i];
;                     if (do_pv) { const u32x2 lo = {vreg[i].x, vreg[i].y}, hi = {vreg[i].z, vreg[i].w};
;                         *(LAS u32x2*)(L + AT_V + i * AT_TS + st_va) = lo; *(LAS u32x2*)(L + AT_V + i * AT_TS + (st_va ^ 16)) = hi; } }
;                 if (rd + 1 < nrounds) AT_ISSUE(rd + 1);
.LBB0_1151:
	v_add_u32_e32 v106, 0, v224
	v_add_u32_e32 v107, 0, v229
	s_waitcnt lgkmcnt(0)
	s_barrier
	s_waitcnt vmcnt(13)
	ds_write_b128 v228, v[2:5]
	s_waitcnt vmcnt(12)
	ds_write_b64 v106, v[6:7] offset:8192
	ds_write_b64 v107, v[8:9] offset:8192
	s_waitcnt vmcnt(11)
	ds_write_b128 v228, v[10:13] offset:16384
	s_waitcnt vmcnt(10)
	ds_write_b64 v106, v[14:15] offset:24576
	ds_write_b64 v107, v[16:17] offset:24576
	s_waitcnt vmcnt(9)
	ds_write_b128 v228, v[18:21] offset:32768
	s_waitcnt vmcnt(8)
	ds_write_b64 v106, v[22:23] offset:40960
	ds_write_b64 v107, v[24:25] offset:40960
	s_waitcnt vmcnt(7)
	ds_write_b128 v228, v[26:29] offset:49152
	s_waitcnt vmcnt(6)
	ds_write_b64 v106, v[30:31] offset:57344
	ds_write_b64 v107, v[32:33] offset:57344
	v_add_u32_e32 v106, 0x10000, v228
	s_waitcnt vmcnt(5)
	ds_write_b128 v106, v[34:37]
	v_add_u32_e32 v106, s26, v224
	s_waitcnt vmcnt(4)
	ds_write_b64 v106, v[38:39]
	v_add_u32_e32 v106, s26, v229
	ds_write_b64 v106, v[40:41]
	v_add_u32_e32 v106, 0x14000, v228
	s_waitcnt vmcnt(3)
	ds_write_b128 v106, v[42:45]
	v_add_u32_e32 v106, s27, v224
	s_waitcnt vmcnt(2)
	ds_write_b64 v106, v[46:47]
	v_add_u32_e32 v106, s27, v229
	ds_write_b64 v106, v[48:49]
	v_add_u32_e32 v106, 0x18000, v228
	s_waitcnt vmcnt(1)
	ds_write_b128 v106, v[50:53]
	v_add_u32_e32 v106, s28, v224
	s_add_i32 s54, s54, 1
	s_waitcnt vmcnt(0)
	ds_write_b64 v106, v[54:55]
	v_add_u32_e32 v106, s28, v229
	s_cmp_ge_i32 s54, s14
	ds_write_b64 v106, v[56:57]
	s_cbranch_scc1 .LBB0_1153
	s_add_i32 s3, s55, -6
	v_mbcnt_lo_u32_b32 v54, -1, 0
	v_mbcnt_hi_u32_b32 v54, -1, v54
	v_add_u32_e32 v54, s3, v54
	v_min_i32_e32 v54, s52, v54
	s_add_i32 s2, 0, 0x25080
	v_lshl_add_u32 v54, v54, 2, s2
	ds_read_b32 v55, v54
	s_waitcnt lgkmcnt(0)
	v_readlane_b32 s4, v55, 0
	s_lshl_b32 s4, s4, 6
	s_cmp_lt_i32 s3, s13
	s_cselect_b32 s56, s4, -1
	s_max_i32 s42, s4, 0
	s_lshl_b64 s[0:1], s[42:43], 13
	s_lshl_b32 s42, s42, 1
	v_lshl_add_u64 v[2:3], v[198:199], 0, s[0:1]
	v_lshl_add_u64 v[6:7], v[200:201], 0, s[42:43]
	global_load_dwordx4 v[2:5], v[2:3], off
	s_nop 0
	global_load_dwordx4 v[6:9], v[6:7], off
	s_add_i32 s3, s3, 1
	v_readlane_b32 s4, v55, 1
	s_lshl_b32 s4, s4, 6
	s_cmp_lt_i32 s3, s13
	s_cselect_b32 s57, s4, -1
	s_max_i32 s42, s4, 0
	s_lshl_b64 s[0:1], s[42:43], 13
	s_lshl_b32 s42, s42, 1
	v_lshl_add_u64 v[10:11], v[198:199], 0, s[0:1]
	v_lshl_add_u64 v[14:15], v[200:201], 0, s[42:43]
	global_load_dwordx4 v[10:13], v[10:11], off
	s_nop 0
	global_load_dwordx4 v[14:17], v[14:15], off
	s_add_i32 s3, s3, 1
	v_readlane_b32 s4, v55, 2
	s_lshl_b32 s4, s4, 6
	s_cmp_lt_i32 s3, s13
	s_cselect_b32 s58, s4, -1
	s_max_i32 s42, s4, 0
	s_lshl_b64 s[0:1], s[42:43], 13
	s_lshl_b32 s42, s42, 1
	v_lshl_add_u64 v[18:19], v[198:199], 0, s[0:1]
	v_lshl_add_u64 v[22:23], v[200:201], 0, s[42:43]
	global_load_dwordx4 v[18:21], v[18:19], off
	s_nop 0
	global_load_dwordx4 v[22:25], v[22:23], off
	s_add_i32 s3, s3, 1
	v_readlane_b32 s4, v55, 3
	s_lshl_b32 s4, s4, 6
	s_cmp_lt_i32 s3, s13
	s_cselect_b32 s59, s4, -1
	s_max_i32 s42, s4, 0
	s_lshl_b64 s[0:1], s[42:43], 13
	s_lshl_b32 s42, s42, 1
	v_lshl_add_u64 v[26:27], v[198:199], 0, s[0:1]
	v_lshl_add_u64 v[30:31], v[200:201], 0, s[42:43]
	global_load_dwordx4 v[26:29], v[26:27], off
	s_nop 0
	global_load_dwordx4 v[30:33], v[30:31], off
	s_add_i32 s3, s3, 1
	v_readlane_b32 s4, v55, 4
	s_lshl_b32 s4, s4, 6
	s_cmp_lt_i32 s3, s13
	s_cselect_b32 s60, s4, -1
	s_max_i32 s42, s4, 0
	s_lshl_b64 s[0:1], s[42:43], 13
	s_lshl_b32 s42, s42, 1
	v_lshl_add_u64 v[34:35], v[198:199], 0, s[0:1]
	v_lshl_add_u64 v[38:39], v[200:201], 0, s[42:43]
	global_load_dwordx4 v[34:37], v[34:35], off
	s_nop 0
	global_load_dwordx4 v[38:41], v[38:39], off
	s_add_i32 s3, s3, 1
	v_readlane_b32 s4, v55, 5
	s_lshl_b32 s4, s4, 6
	s_cmp_lt_i32 s3, s13
	s_cselect_b32 s61, s4, -1
	s_max_i32 s42, s4, 0
	s_lshl_b64 s[0:1], s[42:43], 13
	s_lshl_b32 s42, s42, 1
	v_lshl_add_u64 v[42:43], v[198:199], 0, s[0:1]
	v_lshl_add_u64 v[46:47], v[200:201], 0, s[42:43]
	global_load_dwordx4 v[42:45], v[42:43], off
	s_nop 0
	global_load_dwordx4 v[46:49], v[46:47], off
	s_add_i32 s3, s3, 1
	v_readlane_b32 s4, v55, 6
	s_lshl_b32 s4, s4, 6
	s_cmp_lt_i32 s3, s13
	s_cselect_b32 s62, s4, -1
	s_max_i32 s42, s4, 0
	s_lshl_b64 s[0:1], s[42:43], 13
	s_lshl_b32 s42, s42, 1
	v_lshl_add_u64 v[50:51], v[198:199], 0, s[0:1]
	v_lshl_add_u64 v[54:55], v[200:201], 0, s[42:43]
	global_load_dwordx4 v[50:53], v[50:51], off
	s_nop 0
	global_load_dwordx4 v[54:57], v[54:55], off
